# adds: GLA chunk unit staging (gla_low + raw q/k tiles) and W2/bias loads issued as one batch of 23 loads before the LDS writes (was 7 serial round trips)
# speedup vs baseline: 1.0139x; 1.0082x over previous
.LBB0_289:
	global_load_dword v199, v[2:3], off
	global_load_dword v198, v[2:3], off offset:2048
	s_lshl_b32 s8, s10, 4
	s_and_b32 s11, s8, 0xfffff800
	s_lshl_b32 s8, s10, 6
	s_ashr_i32 s18, s10, 5
	s_and_b32 s8, s8, 0x7c0
	s_lshl_b32 s14, s18, 7
	s_or_b32 s11, s11, s8
	s_and_b32 s33, s14, 0x180
	s_lshl_b32 s19, s33, 1
	v_readlane_b32 s14, v254, 38
	v_or_b32_e32 v2, s11, v1
	s_add_u32 s14, s14, s19
	v_readlane_b32 s15, v254, 40
	v_ashrrev_i32_e32 v3, 31, v2
	s_addc_u32 s15, s15, 0
	v_lshlrev_b64 v[2:3], 10, v[2:3]
	v_lshl_add_u64 v[226:227], s[14:15], 0, v[2:3]
	v_lshl_add_u64 v[226:227], v[226:227], 0, v[34:35]
	global_load_dwordx4 v[200:203], v[226:227], off
	v_readlane_b32 vcc_lo, v254, 42
	s_add_u32 vcc_lo, vcc_lo, s19
	v_readlane_b32 vcc_hi, v254, 44
	s_addc_u32 vcc_hi, vcc_hi, 0
	v_lshl_add_u64 v[228:229], vcc, 0, v[2:3]
	v_lshl_add_u64 v[228:229], v[228:229], 0, v[34:35]
	global_load_dwordx4 v[204:207], v[228:229], off
	v_or_b32_e32 v4, s11, v73
	v_ashrrev_i32_e32 v5, 31, v4
	v_lshlrev_b64 v[4:5], 10, v[4:5]
	v_lshl_add_u64 v[230:231], s[14:15], 0, v[4:5]
	v_lshl_add_u64 v[230:231], v[230:231], 0, v[34:35]
	global_load_dwordx4 v[218:221], v[230:231], off
	v_lshl_add_u64 v[232:233], vcc, 0, v[4:5]
	v_lshl_add_u64 v[232:233], v[232:233], 0, v[34:35]
	global_load_dwordx4 v[222:225], v[232:233], off
	s_movk_i32 s11, 0x1000
	v_readlane_b32 s14, v254, 58
	v_readlane_b32 s15, v254, 59
	v_or_b32_e32 v6, s33, v76
	v_lshlrev_b32_e32 v6, 2, v6
	v_mov_b32_e32 v7, v35
	v_lshl_add_u64 v[22:23], s[56:57], 0, v[6:7]
	v_add_co_u32_e32 v8, vcc, s11, v22
	s_movk_i32 s11, 0x2000
	s_nop 0
	v_addc_co_u32_e32 v9, vcc, 0, v23, vcc
	v_add_co_u32_e32 v10, vcc, s11, v22
	s_movk_i32 s11, 0x3000
	s_nop 0
	v_addc_co_u32_e32 v11, vcc, 0, v23, vcc
	global_load_dword v14, v6, s[56:57]
	global_load_dword v15, v6, s[56:57] offset:2048
	global_load_dword v16, v[10:11], off offset:-4096
	global_load_dword v17, v[8:9], off offset:2048
	global_load_dword v7, v[10:11], off
	s_nop 0
	global_load_dword v8, v[10:11], off offset:2048
	v_add_co_u32_e32 v10, vcc, s11, v22
	s_movk_i32 s11, 0x4000
	s_nop 0
	v_addc_co_u32_e32 v11, vcc, 0, v23, vcc
	v_add_co_u32_e32 v18, vcc, s11, v22
	s_movk_i32 s11, 0x5000
	s_nop 0
	v_addc_co_u32_e32 v19, vcc, 0, v23, vcc
	v_add_co_u32_e32 v20, vcc, s11, v22
	s_movk_i32 s11, 0x6000
	s_nop 0
	v_addc_co_u32_e32 v21, vcc, 0, v23, vcc
	v_add_co_u32_e32 v24, vcc, s11, v22
	s_movk_i32 s11, 0x7000
	s_nop 0
	v_addc_co_u32_e32 v25, vcc, 0, v23, vcc
	global_load_dword v12, v[18:19], off offset:-4096
	global_load_dword v13, v[10:11], off offset:2048
	global_load_dword v9, v[18:19], off
	s_nop 0
	global_load_dword v10, v[18:19], off offset:2048
	s_nop 0
	global_load_dword v19, v[24:25], off offset:-4096
	s_nop 0
	global_load_dword v20, v[20:21], off offset:2048
	s_nop 0
	global_load_dword v11, v[24:25], off
	global_load_dword v18, v[24:25], off offset:2048
	v_add_co_u32_e32 v24, vcc, s11, v22
	s_mov_b32 s11, 0xbd800000
	s_nop 0
	v_addc_co_u32_e32 v25, vcc, 0, v23, vcc
	global_load_dword v22, v[24:25], off
	global_load_dword v21, v[24:25], off offset:2048
	s_nop 0
	global_load_dword v24, v6, s[58:59]
	s_waitcnt vmcnt(22)
	ds_write_b32 v147, v199
	s_waitcnt vmcnt(21)
	ds_write_b32 v147, v198 offset:2048
	s_waitcnt vmcnt(20)
	ds_write_b128 v71, v[200:203] offset:59392
	s_waitcnt vmcnt(19)
	ds_write_b128 v72, v[204:207]
	s_waitcnt vmcnt(18)
	ds_write_b128 v74, v[218:221] offset:59392
	s_waitcnt vmcnt(17)
	ds_write_b128 v75, v[222:225]
	s_waitcnt lgkmcnt(0)
	s_barrier
	ds_read_b128 v[26:29], v77 offset:53248
	ds_read_b128 v[30:33], v77 offset:53264
	ds_read_b128 v[64:67], v77 offset:53280
	ds_read_b128 v[150:153], v77 offset:53296
	s_waitcnt vmcnt(15) lgkmcnt(3)
	v_mul_f32_e32 v6, v15, v27
	v_fmac_f32_e32 v6, v14, v26
	s_waitcnt vmcnt(11) lgkmcnt(2)
	v_mul_f32_e32 v23, v8, v31
	v_fmac_f32_e32 v6, v16, v28
	v_fmac_f32_e32 v23, v7, v30
	v_fmac_f32_e32 v6, v17, v29
	ds_read_b128 v[26:29], v77 offset:53312
	s_waitcnt vmcnt(10)
	v_fmac_f32_e32 v23, v12, v32
	s_waitcnt vmcnt(9)
	v_fmac_f32_e32 v23, v13, v33
	s_waitcnt vmcnt(0)
	v_add_f32_e32 v6, v24, v6
	v_add_f32_e32 v6, v6, v23
	s_waitcnt lgkmcnt(2)
	v_mul_f32_e32 v23, v10, v65
	v_fmac_f32_e32 v23, v9, v64
	v_fmac_f32_e32 v23, v19, v66
	v_fmac_f32_e32 v23, v20, v67
	v_add_f32_e32 v6, v6, v23
	s_waitcnt lgkmcnt(1)
	v_mul_f32_e32 v23, v18, v151
	v_fmac_f32_e32 v23, v11, v150
	v_fmac_f32_e32 v23, v22, v152
	v_fmac_f32_e32 v23, v21, v153
	v_add_f32_e32 v6, v6, v23
	v_mul_f32_e32 v6, 0x3fb8aa3b, v6
	v_max_f32_e64 v23, -v6, 0
	v_exp_f32_e64 v6, -|v6|
	ds_read_b128 v[64:67], v77 offset:53760
	ds_read_b128 v[150:153], v77 offset:54208
	v_add_f32_e32 v6, 1.0, v6
	v_log_f32_e32 v6, v6
	s_nop 0
	v_add_f32_e32 v6, v23, v6
	s_waitcnt lgkmcnt(2)
	v_mul_f32_e32 v23, v15, v27
	v_fmac_f32_e32 v23, v14, v26
	v_fmac_f32_e32 v23, v16, v28
	v_fmac_f32_e32 v23, v17, v29
	ds_read_b128 v[26:29], v77 offset:53328
	v_add_f32_e32 v23, v24, v23
	v_fma_f32 v6, v6, s11, 0
	s_waitcnt lgkmcnt(0)
	v_mul_f32_e32 v25, v8, v27
	v_fmac_f32_e32 v25, v7, v26
	v_fmac_f32_e32 v25, v12, v28
	v_fmac_f32_e32 v25, v13, v29
	ds_read_b128 v[26:29], v77 offset:53344
	v_add_f32_e32 v23, v23, v25
	s_waitcnt lgkmcnt(0)
	v_mul_f32_e32 v25, v10, v27
	v_fmac_f32_e32 v25, v9, v26
	v_fmac_f32_e32 v25, v19, v28
	v_fmac_f32_e32 v25, v20, v29
	ds_read_b128 v[26:29], v77 offset:53360
	v_add_f32_e32 v23, v23, v25
	s_waitcnt lgkmcnt(0)
	v_mul_f32_e32 v25, v18, v27
	v_fmac_f32_e32 v25, v11, v26
	v_fmac_f32_e32 v25, v22, v28
	v_fmac_f32_e32 v25, v21, v29
	v_add_f32_e32 v23, v23, v25
	v_mul_f32_e32 v23, 0x3fb8aa3b, v23
	v_max_f32_e64 v25, -v23, 0
	v_exp_f32_e64 v23, -|v23|
	ds_read_b128 v[26:29], v77 offset:53376
	v_add_f32_e32 v23, 1.0, v23
	v_log_f32_e32 v23, v23
	s_nop 0
	v_add_f32_e32 v23, v25, v23
	s_waitcnt lgkmcnt(0)
	v_mul_f32_e32 v25, v15, v27
	v_fmac_f32_e32 v25, v14, v26
	v_fmac_f32_e32 v25, v16, v28
	v_fmac_f32_e32 v25, v17, v29
	ds_read_b128 v[26:29], v77 offset:53392
	v_add_f32_e32 v25, v24, v25
	v_fmamk_f32 v23, v23, 0xbd800000, v6
	s_waitcnt lgkmcnt(0)
	v_mul_f32_e32 v27, v8, v27
	v_fmac_f32_e32 v27, v7, v26
	v_fmac_f32_e32 v27, v12, v28
	v_fmac_f32_e32 v27, v13, v29
	v_add_f32_e32 v25, v25, v27
	ds_read_b128 v[26:29], v77 offset:53408
	s_waitcnt lgkmcnt(0)
	v_mul_f32_e32 v27, v10, v27
	v_fmac_f32_e32 v27, v9, v26
	v_fmac_f32_e32 v27, v19, v28
	v_fmac_f32_e32 v27, v20, v29
	v_add_f32_e32 v25, v25, v27
	ds_read_b128 v[26:29], v77 offset:53424
	s_waitcnt lgkmcnt(0)
	v_mul_f32_e32 v27, v18, v27
	v_fmac_f32_e32 v27, v11, v26
	v_fmac_f32_e32 v27, v22, v28
	v_fmac_f32_e32 v27, v21, v29
	v_add_f32_e32 v25, v25, v27
	v_mul_f32_e32 v25, 0x3fb8aa3b, v25
	v_max_f32_e64 v26, -v25, 0
	v_exp_f32_e64 v25, -|v25|
	s_nop 0
	v_add_f32_e32 v25, 1.0, v25
	v_log_f32_e32 v25, v25
	s_nop 0
	v_add_f32_e32 v25, v26, v25
	ds_read_b128 v[26:29], v77 offset:53440
	v_fmamk_f32 v25, v25, 0xbd800000, v23
	s_waitcnt lgkmcnt(0)
	v_mul_f32_e32 v27, v15, v27
	v_fmac_f32_e32 v27, v14, v26
	v_fmac_f32_e32 v27, v16, v28
	v_fmac_f32_e32 v27, v17, v29
	v_add_f32_e32 v30, v24, v27
	ds_read_b128 v[26:29], v77 offset:53456
	s_waitcnt lgkmcnt(0)
	v_mul_f32_e32 v27, v8, v27
	v_fmac_f32_e32 v27, v7, v26
	v_fmac_f32_e32 v27, v12, v28
	v_fmac_f32_e32 v27, v13, v29
	v_add_f32_e32 v30, v30, v27
	ds_read_b128 v[26:29], v77 offset:53472
	s_waitcnt lgkmcnt(0)
	v_mul_f32_e32 v27, v10, v27
	v_fmac_f32_e32 v27, v9, v26
	v_fmac_f32_e32 v27, v19, v28
	v_fmac_f32_e32 v27, v20, v29
	v_add_f32_e32 v30, v30, v27
	ds_read_b128 v[26:29], v77 offset:53488
	s_waitcnt lgkmcnt(0)
	v_mul_f32_e32 v27, v18, v27
	v_fmac_f32_e32 v27, v11, v26
	v_fmac_f32_e32 v27, v22, v28
	v_fmac_f32_e32 v27, v21, v29
	v_add_f32_e32 v26, v30, v27
	v_mul_f32_e32 v26, 0x3fb8aa3b, v26
	v_max_f32_e64 v27, -v26, 0
	v_exp_f32_e64 v26, -|v26|
	ds_read_b128 v[28:31], v77 offset:53504
	v_add_f32_e32 v26, 1.0, v26
	v_log_f32_e32 v26, v26
	s_nop 0
	v_add_f32_e32 v26, v27, v26
	s_waitcnt lgkmcnt(0)
	v_mul_f32_e32 v27, v15, v29
	v_fmac_f32_e32 v27, v14, v28
	v_fmac_f32_e32 v27, v16, v30
	v_fmac_f32_e32 v27, v17, v31
	ds_read_b128 v[28:31], v77 offset:53520
	v_add_f32_e32 v27, v24, v27
	v_fmamk_f32 v26, v26, 0xbd800000, v25
	s_waitcnt lgkmcnt(0)
	v_mul_f32_e32 v29, v8, v29
	v_fmac_f32_e32 v29, v7, v28
	v_fmac_f32_e32 v29, v12, v30
	v_fmac_f32_e32 v29, v13, v31
	v_add_f32_e32 v27, v27, v29
	ds_read_b128 v[28:31], v77 offset:53536
	s_waitcnt lgkmcnt(0)
	v_mul_f32_e32 v29, v10, v29
	v_fmac_f32_e32 v29, v9, v28
	v_fmac_f32_e32 v29, v19, v30
	v_fmac_f32_e32 v29, v20, v31
	v_add_f32_e32 v27, v27, v29
	ds_read_b128 v[28:31], v77 offset:53552
	s_waitcnt lgkmcnt(0)
	v_mul_f32_e32 v29, v18, v29
	v_fmac_f32_e32 v29, v11, v28
	v_fmac_f32_e32 v29, v22, v30
	v_fmac_f32_e32 v29, v21, v31
	v_add_f32_e32 v27, v27, v29
	v_mul_f32_e32 v27, 0x3fb8aa3b, v27
	v_max_f32_e64 v28, -v27, 0
	v_exp_f32_e64 v27, -|v27|
	s_nop 0
	v_add_f32_e32 v27, 1.0, v27
	v_log_f32_e32 v27, v27
	s_nop 0
	v_add_f32_e32 v27, v28, v27
	ds_read_b128 v[28:31], v77 offset:53568
	v_fmamk_f32 v27, v27, 0xbd800000, v26
	s_waitcnt lgkmcnt(0)
	v_mul_f32_e32 v29, v15, v29
	v_fmac_f32_e32 v29, v14, v28
	v_fmac_f32_e32 v29, v16, v30
	v_fmac_f32_e32 v29, v17, v31
	v_add_f32_e32 v32, v24, v29
	ds_read_b128 v[28:31], v77 offset:53584
	s_waitcnt lgkmcnt(0)
	v_mul_f32_e32 v29, v8, v29
	v_fmac_f32_e32 v29, v7, v28
	v_fmac_f32_e32 v29, v12, v30
	v_fmac_f32_e32 v29, v13, v31
	v_add_f32_e32 v32, v32, v29
	ds_read_b128 v[28:31], v77 offset:53600
	s_waitcnt lgkmcnt(0)
	v_mul_f32_e32 v29, v10, v29
	v_fmac_f32_e32 v29, v9, v28
	v_fmac_f32_e32 v29, v19, v30
	v_fmac_f32_e32 v29, v20, v31
	v_add_f32_e32 v32, v32, v29
	ds_read_b128 v[28:31], v77 offset:53616
	s_waitcnt lgkmcnt(0)
	v_mul_f32_e32 v29, v18, v29
	v_fmac_f32_e32 v29, v11, v28
	v_fmac_f32_e32 v29, v22, v30
	v_fmac_f32_e32 v29, v21, v31
	v_add_f32_e32 v28, v32, v29
	v_mul_f32_e32 v28, 0x3fb8aa3b, v28
	v_max_f32_e64 v29, -v28, 0
	v_exp_f32_e64 v28, -|v28|
	ds_read_b128 v[30:33], v77 offset:53632
	v_add_f32_e32 v28, 1.0, v28
	v_log_f32_e32 v28, v28
	s_nop 0
	v_add_f32_e32 v28, v29, v28
	s_waitcnt lgkmcnt(0)
	v_mul_f32_e32 v29, v15, v31
	v_fmac_f32_e32 v29, v14, v30
	v_fmac_f32_e32 v29, v16, v32
	v_fmac_f32_e32 v29, v17, v33
	ds_read_b128 v[30:33], v77 offset:53648
	v_add_f32_e32 v29, v24, v29
	v_fmamk_f32 v28, v28, 0xbd800000, v27
	s_waitcnt lgkmcnt(0)
	v_mul_f32_e32 v31, v8, v31
	v_fmac_f32_e32 v31, v7, v30
	v_fmac_f32_e32 v31, v12, v32
	v_fmac_f32_e32 v31, v13, v33
	v_add_f32_e32 v29, v29, v31
	ds_read_b128 v[30:33], v77 offset:53664
	s_waitcnt lgkmcnt(0)
	v_mul_f32_e32 v31, v10, v31
	v_fmac_f32_e32 v31, v9, v30
	v_fmac_f32_e32 v31, v19, v32
	v_fmac_f32_e32 v31, v20, v33
	v_add_f32_e32 v29, v29, v31
	ds_read_b128 v[30:33], v77 offset:53680
	s_waitcnt lgkmcnt(0)
	v_mul_f32_e32 v31, v18, v31
	v_fmac_f32_e32 v31, v11, v30
	v_fmac_f32_e32 v31, v22, v32
	v_fmac_f32_e32 v31, v21, v33
	v_add_f32_e32 v29, v29, v31
	v_mul_f32_e32 v29, 0x3fb8aa3b, v29
	v_max_f32_e64 v30, -v29, 0
	v_exp_f32_e64 v29, -|v29|
	s_nop 0
	v_add_f32_e32 v29, 1.0, v29
	v_log_f32_e32 v29, v29
	s_nop 0
	v_add_f32_e32 v29, v30, v29
	ds_read_b128 v[30:33], v77 offset:53696
	v_fmamk_f32 v29, v29, 0xbd800000, v28
	s_waitcnt lgkmcnt(0)
	v_mul_f32_e32 v31, v15, v31
	v_fmac_f32_e32 v31, v14, v30
	v_fmac_f32_e32 v31, v16, v32
	v_fmac_f32_e32 v31, v17, v33
	v_add_f32_e32 v63, v24, v31
	ds_read_b128 v[30:33], v77 offset:53712
	s_waitcnt lgkmcnt(0)
	v_mul_f32_e32 v31, v8, v31
	v_fmac_f32_e32 v31, v7, v30
	v_fmac_f32_e32 v31, v12, v32
	v_fmac_f32_e32 v31, v13, v33
	v_add_f32_e32 v63, v63, v31
	ds_read_b128 v[30:33], v77 offset:53728
	s_waitcnt lgkmcnt(0)
	v_mul_f32_e32 v31, v10, v31
	v_fmac_f32_e32 v31, v9, v30
	v_fmac_f32_e32 v31, v19, v32
	v_fmac_f32_e32 v31, v20, v33
	v_add_f32_e32 v63, v63, v31
	ds_read_b128 v[30:33], v77 offset:53744
	s_waitcnt lgkmcnt(0)
	v_mul_f32_e32 v31, v18, v31
	v_fmac_f32_e32 v31, v11, v30
	v_fmac_f32_e32 v31, v22, v32
	v_fmac_f32_e32 v31, v21, v33
	v_add_f32_e32 v30, v63, v31
	v_mul_f32_e32 v30, 0x3fb8aa3b, v30
	v_max_f32_e64 v31, -v30, 0
	v_exp_f32_e64 v30, -|v30|
	s_nop 0
	v_add_f32_e32 v30, 1.0, v30
	v_log_f32_e32 v30, v30
	s_nop 0
	v_add_f32_e32 v30, v31, v30
	v_mul_f32_e32 v31, v15, v65
	v_fmac_f32_e32 v31, v14, v64
	v_fmac_f32_e32 v31, v16, v66
	v_fmac_f32_e32 v31, v17, v67
	ds_read_b128 v[64:67], v77 offset:53776
	v_add_f32_e32 v31, v24, v31
	v_fmamk_f32 v30, v30, 0xbd800000, v29
	s_waitcnt lgkmcnt(0)
	v_mul_f32_e32 v32, v8, v65
	v_fmac_f32_e32 v32, v7, v64
	v_fmac_f32_e32 v32, v12, v66
	v_fmac_f32_e32 v32, v13, v67
	ds_read_b128 v[64:67], v77 offset:53792
	v_add_f32_e32 v31, v31, v32
	s_waitcnt lgkmcnt(0)
	v_mul_f32_e32 v32, v10, v65
	v_fmac_f32_e32 v32, v9, v64
	v_fmac_f32_e32 v32, v19, v66
	v_fmac_f32_e32 v32, v20, v67
	ds_read_b128 v[64:67], v77 offset:53808
	v_add_f32_e32 v31, v31, v32
	s_waitcnt lgkmcnt(0)
	v_mul_f32_e32 v32, v18, v65
	v_fmac_f32_e32 v32, v11, v64
	v_fmac_f32_e32 v32, v22, v66
	v_fmac_f32_e32 v32, v21, v67
	v_add_f32_e32 v31, v31, v32
	v_mul_f32_e32 v31, 0x3fb8aa3b, v31
	v_max_f32_e64 v32, -v31, 0
	v_exp_f32_e64 v31, -|v31|
	ds_read_b128 v[64:67], v77 offset:53824
	v_add_f32_e32 v31, 1.0, v31
	v_log_f32_e32 v31, v31
	s_nop 0
	v_add_f32_e32 v31, v32, v31
	s_waitcnt lgkmcnt(0)
	v_mul_f32_e32 v32, v15, v65
	v_fmac_f32_e32 v32, v14, v64
	v_fmac_f32_e32 v32, v16, v66
	v_fmac_f32_e32 v32, v17, v67
	ds_read_b128 v[64:67], v77 offset:53840
	v_add_f32_e32 v32, v24, v32
	v_fmamk_f32 v31, v31, 0xbd800000, v30
	s_waitcnt lgkmcnt(0)
	v_mul_f32_e32 v33, v8, v65
	v_fmac_f32_e32 v33, v7, v64
	v_fmac_f32_e32 v33, v12, v66
	v_fmac_f32_e32 v33, v13, v67
	ds_read_b128 v[64:67], v77 offset:53856
	v_add_f32_e32 v32, v32, v33
	s_waitcnt lgkmcnt(0)
	v_mul_f32_e32 v33, v10, v65
	v_fmac_f32_e32 v33, v9, v64
	v_fmac_f32_e32 v33, v19, v66
	v_fmac_f32_e32 v33, v20, v67
	ds_read_b128 v[64:67], v77 offset:53872
	v_add_f32_e32 v32, v32, v33
	s_waitcnt lgkmcnt(0)
	v_mul_f32_e32 v33, v18, v65
	v_fmac_f32_e32 v33, v11, v64
	v_fmac_f32_e32 v33, v22, v66
	v_fmac_f32_e32 v33, v21, v67
	v_add_f32_e32 v32, v32, v33
	v_mul_f32_e32 v32, 0x3fb8aa3b, v32
	v_max_f32_e64 v33, -v32, 0
	v_exp_f32_e64 v32, -|v32|
	ds_read_b128 v[64:67], v77 offset:53888
	v_add_f32_e32 v32, 1.0, v32
	v_log_f32_e32 v32, v32
	s_nop 0
	v_add_f32_e32 v32, v33, v32
	s_waitcnt lgkmcnt(0)
	v_mul_f32_e32 v33, v15, v65
	v_fmac_f32_e32 v33, v14, v64
	v_fmac_f32_e32 v33, v16, v66
	v_fmac_f32_e32 v33, v17, v67
	ds_read_b128 v[64:67], v77 offset:53904
	v_add_f32_e32 v33, v24, v33
	v_fmamk_f32 v32, v32, 0xbd800000, v31
	s_waitcnt lgkmcnt(0)
	v_mul_f32_e32 v63, v8, v65
	v_fmac_f32_e32 v63, v7, v64
	v_fmac_f32_e32 v63, v12, v66
	v_fmac_f32_e32 v63, v13, v67
	ds_read_b128 v[64:67], v77 offset:53920
	v_add_f32_e32 v33, v33, v63
	s_waitcnt lgkmcnt(0)
	v_mul_f32_e32 v63, v10, v65
	v_fmac_f32_e32 v63, v9, v64
	v_fmac_f32_e32 v63, v19, v66
	v_fmac_f32_e32 v63, v20, v67
	ds_read_b128 v[64:67], v77 offset:53936
	v_add_f32_e32 v33, v33, v63
	s_waitcnt lgkmcnt(0)
	v_mul_f32_e32 v63, v18, v65
	v_fmac_f32_e32 v63, v11, v64
	v_fmac_f32_e32 v63, v22, v66
	v_fmac_f32_e32 v63, v21, v67
	v_add_f32_e32 v33, v33, v63
	v_mul_f32_e32 v33, 0x3fb8aa3b, v33
	v_max_f32_e64 v63, -v33, 0
	v_exp_f32_e64 v33, -|v33|
	ds_read_b128 v[64:67], v77 offset:53952
	v_add_f32_e32 v33, 1.0, v33
	v_log_f32_e32 v33, v33
	s_nop 0
	v_add_f32_e32 v33, v63, v33
	s_waitcnt lgkmcnt(0)
	v_mul_f32_e32 v63, v15, v65
	v_fmac_f32_e32 v63, v14, v64
	v_fmac_f32_e32 v63, v16, v66
	v_fmac_f32_e32 v63, v17, v67
	ds_read_b128 v[64:67], v77 offset:53968
	v_add_f32_e32 v63, v24, v63
	v_fmamk_f32 v33, v33, 0xbd800000, v32
	s_waitcnt lgkmcnt(0)
	v_mul_f32_e32 v65, v8, v65
	v_fmac_f32_e32 v65, v7, v64
	v_fmac_f32_e32 v65, v12, v66
	v_fmac_f32_e32 v65, v13, v67
	v_add_f32_e32 v63, v63, v65
	ds_read_b128 v[64:67], v77 offset:53984
	s_waitcnt lgkmcnt(0)
	v_mul_f32_e32 v65, v10, v65
	v_fmac_f32_e32 v65, v9, v64
	v_fmac_f32_e32 v65, v19, v66
	v_fmac_f32_e32 v65, v20, v67
	v_add_f32_e32 v63, v63, v65
	ds_read_b128 v[64:67], v77 offset:54000
	s_waitcnt lgkmcnt(0)
	v_mul_f32_e32 v65, v18, v65
	v_fmac_f32_e32 v65, v11, v64
	v_fmac_f32_e32 v65, v22, v66
	v_fmac_f32_e32 v65, v21, v67
	v_add_f32_e32 v63, v63, v65
	v_mul_f32_e32 v63, 0x3fb8aa3b, v63
	v_max_f32_e64 v64, -v63, 0
	v_exp_f32_e64 v63, -|v63|
	s_nop 0
	v_add_f32_e32 v63, 1.0, v63
	v_log_f32_e32 v63, v63
	s_nop 0
	v_add_f32_e32 v63, v64, v63
	ds_read_b128 v[64:67], v77 offset:54016
	v_fmamk_f32 v63, v63, 0xbd800000, v33
	s_waitcnt lgkmcnt(0)
	v_mul_f32_e32 v65, v15, v65
	v_fmac_f32_e32 v65, v14, v64
	v_fmac_f32_e32 v65, v16, v66
	v_fmac_f32_e32 v65, v17, v67
	v_add_f32_e32 v68, v24, v65
	ds_read_b128 v[64:67], v77 offset:54032
	s_waitcnt lgkmcnt(0)
	v_mul_f32_e32 v65, v8, v65
	v_fmac_f32_e32 v65, v7, v64
	v_fmac_f32_e32 v65, v12, v66
	v_fmac_f32_e32 v65, v13, v67
	v_add_f32_e32 v68, v68, v65
	ds_read_b128 v[64:67], v77 offset:54048
	s_waitcnt lgkmcnt(0)
	v_mul_f32_e32 v65, v10, v65
	v_fmac_f32_e32 v65, v9, v64
	v_fmac_f32_e32 v65, v19, v66
	v_fmac_f32_e32 v65, v20, v67
	v_add_f32_e32 v68, v68, v65
	ds_read_b128 v[64:67], v77 offset:54064
	s_waitcnt lgkmcnt(0)
	v_mul_f32_e32 v65, v18, v65
	v_fmac_f32_e32 v65, v11, v64
	v_fmac_f32_e32 v65, v22, v66
	v_fmac_f32_e32 v65, v21, v67
	v_add_f32_e32 v64, v68, v65
	v_mul_f32_e32 v64, 0x3fb8aa3b, v64
	v_max_f32_e64 v65, -v64, 0
	v_exp_f32_e64 v64, -|v64|
	ds_read_b128 v[66:69], v77 offset:54080
	v_add_f32_e32 v64, 1.0, v64
	v_log_f32_e32 v64, v64
	s_nop 0
	v_add_f32_e32 v64, v65, v64
	s_waitcnt lgkmcnt(0)
	v_mul_f32_e32 v65, v15, v67
	v_fmac_f32_e32 v65, v14, v66
	v_fmac_f32_e32 v65, v16, v68
	v_fmac_f32_e32 v65, v17, v69
	ds_read_b128 v[66:69], v77 offset:54096
	v_add_f32_e32 v65, v24, v65
	v_fmamk_f32 v64, v64, 0xbd800000, v63
	s_waitcnt lgkmcnt(0)
	v_mul_f32_e32 v67, v8, v67
	v_fmac_f32_e32 v67, v7, v66
	v_fmac_f32_e32 v67, v12, v68
	v_fmac_f32_e32 v67, v13, v69
	v_add_f32_e32 v65, v65, v67
	ds_read_b128 v[66:69], v77 offset:54112
	s_waitcnt lgkmcnt(0)
	v_mul_f32_e32 v67, v10, v67
	v_fmac_f32_e32 v67, v9, v66
	v_fmac_f32_e32 v67, v19, v68
	v_fmac_f32_e32 v67, v20, v69
	v_add_f32_e32 v65, v65, v67
	ds_read_b128 v[66:69], v77 offset:54128
	s_waitcnt lgkmcnt(0)
	v_mul_f32_e32 v67, v18, v67
	v_fmac_f32_e32 v67, v11, v66
	v_fmac_f32_e32 v67, v22, v68
	v_fmac_f32_e32 v67, v21, v69
	v_add_f32_e32 v65, v65, v67
	v_mul_f32_e32 v65, 0x3fb8aa3b, v65
	v_max_f32_e64 v66, -v65, 0
	v_exp_f32_e64 v65, -|v65|
	s_nop 0
	v_add_f32_e32 v65, 1.0, v65
	v_log_f32_e32 v65, v65
	s_nop 0
	v_add_f32_e32 v65, v66, v65
	ds_read_b128 v[66:69], v77 offset:54144
	v_fmamk_f32 v65, v65, 0xbd800000, v64
	s_waitcnt lgkmcnt(0)
	v_mul_f32_e32 v67, v15, v67
	v_fmac_f32_e32 v67, v14, v66
	v_fmac_f32_e32 v67, v16, v68
	v_fmac_f32_e32 v67, v17, v69
	v_mul_f32_e32 v15, v15, v151
	v_add_f32_e32 v149, v24, v67
	ds_read_b128 v[66:69], v77 offset:54160
	v_fmac_f32_e32 v15, v14, v150
	v_fmac_f32_e32 v15, v16, v152
	v_fmac_f32_e32 v15, v17, v153
	v_add_f32_e32 v24, v24, v15
	ds_read_b128 v[14:17], v77 offset:54224
	s_waitcnt lgkmcnt(1)
	v_mul_f32_e32 v67, v8, v67
	v_fmac_f32_e32 v67, v7, v66
	v_fmac_f32_e32 v67, v12, v68
	v_fmac_f32_e32 v67, v13, v69
	s_waitcnt lgkmcnt(0)
	v_mul_f32_e32 v8, v8, v15
	v_add_f32_e32 v149, v149, v67
	ds_read_b128 v[66:69], v77 offset:54176
	v_fmac_f32_e32 v8, v7, v14
	v_fmac_f32_e32 v8, v12, v16
	v_fmac_f32_e32 v8, v13, v17
	ds_read_b128 v[12:15], v77 offset:54240
	s_waitcnt lgkmcnt(1)
	v_mul_f32_e32 v67, v10, v67
	v_fmac_f32_e32 v67, v9, v66
	v_fmac_f32_e32 v67, v19, v68
	v_add_f32_e32 v7, v24, v8
	s_waitcnt lgkmcnt(0)
	v_mul_f32_e32 v8, v10, v13
	v_fmac_f32_e32 v67, v20, v69
	v_fmac_f32_e32 v8, v9, v12
	v_add_f32_e32 v149, v149, v67
	ds_read_b128 v[66:69], v77 offset:54192
	v_fmac_f32_e32 v8, v19, v14
	v_fmac_f32_e32 v8, v20, v15
	ds_read_b128 v[12:15], v77 offset:54256
	v_add_f32_e32 v7, v7, v8
	s_waitcnt lgkmcnt(1)
	v_mul_f32_e32 v67, v18, v67
	v_fmac_f32_e32 v67, v11, v66
	v_fmac_f32_e32 v67, v22, v68
	s_waitcnt lgkmcnt(0)
	v_mul_f32_e32 v8, v18, v13
	v_fmac_f32_e32 v8, v11, v12
	v_fmac_f32_e32 v67, v21, v69
	v_fmac_f32_e32 v8, v22, v14
	v_add_f32_e32 v66, v149, v67
	v_fmac_f32_e32 v8, v21, v15
	v_mul_f32_e32 v66, 0x3fb8aa3b, v66
	v_add_f32_e32 v7, v7, v8
	v_max_f32_e64 v67, -v66, 0
	v_exp_f32_e64 v66, -|v66|
	v_mul_f32_e32 v7, 0x3fb8aa3b, v7
	v_max_f32_e64 v8, -v7, 0
	v_exp_f32_e64 v7, -|v7|
	v_add_f32_e32 v66, 1.0, v66
	v_log_f32_e32 v66, v66
	v_add_f32_e32 v7, 1.0, v7
	v_log_f32_e32 v7, v7
	v_add_f32_e32 v66, v67, v66
	v_fmamk_f32 v66, v66, 0xbd800000, v65
	v_add_f32_e32 v7, v8, v7
	v_fmamk_f32 v8, v7, 0xbd800000, v66
	ds_write_b32 v78, v8 offset:57344
	s_waitcnt lgkmcnt(0)
	s_barrier
	ds_read2st64_b32 v[10:11], v79 offset0:224 offset1:226
	s_waitcnt lgkmcnt(0)
	v_add_f32_e32 v7, 0, v10
	v_cndmask_b32_e64 v9, v7, 0, s[14:15]
	v_readlane_b32 s14, v254, 62
	v_add_f32_e32 v10, v11, v9
	v_readlane_b32 s15, v254, 63
	v_add_f32_e32 v7, v7, v11
	s_nop 0
	v_cndmask_b32_e64 v9, v9, v10, s[14:15]
	ds_read2st64_b32 v[10:11], v79 offset0:228 offset1:230
	v_readlane_b32 s14, v255, 0
	v_readlane_b32 s15, v255, 1
	s_waitcnt lgkmcnt(0)
	v_add_f32_e32 v7, v7, v10
	v_add_f32_e32 v10, v10, v9
	v_cndmask_b32_e64 v9, v9, v10, s[14:15]
	v_readlane_b32 s14, v255, 2
	v_add_f32_e32 v10, v11, v9
	v_readlane_b32 s15, v255, 3
	v_add_f32_e32 v7, v7, v11
	ds_read_u16 v11, v81
	v_cndmask_b32_e64 v9, v9, v10, s[14:15]
	ds_read_u16 v10, v80 offset:59392
	v_add_f32_e32 v6, v6, v9
	v_exp_f32_e32 v12, v6
	s_waitcnt lgkmcnt(1)
	v_lshlrev_b32_e32 v11, 16, v11
	s_waitcnt lgkmcnt(0)
	v_lshlrev_b32_e32 v10, 16, v10
	v_mul_f32_e32 v10, 0x3db504f3, v10
	v_mul_f32_e32 v10, v10, v12
	v_cvt_pk_bf16_f32 v10, v10, s0
	ds_write_b16 v82, v10
	v_exp_f32_e64 v10, -v6
	v_sub_f32_e32 v6, v7, v6
	v_exp_f32_e32 v6, v6
	v_mul_f32_e32 v10, v10, v11
	v_cvt_pk_bf16_f32 v10, v10, s0
	v_mul_f32_e32 v6, v6, v11
	v_cvt_pk_bf16_f32 v6, v6, s0
	ds_write_b16 v82, v10 offset:17408
	ds_write_b16 v83, v6 offset:34816
	ds_read_u16 v10, v84 offset:59392
	ds_read_u16 v11, v85
	v_add_f32_e32 v6, v23, v9
	v_exp_f32_e32 v12, v6
	s_waitcnt lgkmcnt(1)
	v_lshlrev_b32_e32 v10, 16, v10
	v_mul_f32_e32 v10, 0x3db504f3, v10
	v_mul_f32_e32 v10, v12, v10
	v_cvt_pk_bf16_f32 v10, v10, s0
	ds_write_b16 v86, v10
	v_exp_f32_e64 v10, -v6
	v_sub_f32_e32 v6, v7, v6
	v_exp_f32_e32 v6, v6
	s_waitcnt lgkmcnt(1)
	v_lshlrev_b32_e32 v11, 16, v11
	v_mul_f32_e32 v10, v10, v11
	v_cvt_pk_bf16_f32 v10, v10, s0
	v_mul_f32_e32 v6, v6, v11
	v_cvt_pk_bf16_f32 v6, v6, s0
	ds_write_b16 v86, v10 offset:17408
	ds_write_b16 v83, v6 offset:34818
	ds_read_u16 v10, v87 offset:59392
	ds_read_u16 v11, v88
	v_add_f32_e32 v6, v25, v9
	v_exp_f32_e32 v12, v6
	s_waitcnt lgkmcnt(1)
	v_lshlrev_b32_e32 v10, 16, v10
	v_mul_f32_e32 v10, 0x3db504f3, v10
	v_mul_f32_e32 v10, v12, v10
	v_cvt_pk_bf16_f32 v10, v10, s0
	ds_write_b16 v89, v10
	v_exp_f32_e64 v10, -v6
	v_sub_f32_e32 v6, v7, v6
	v_exp_f32_e32 v6, v6
	s_waitcnt lgkmcnt(1)
	v_lshlrev_b32_e32 v11, 16, v11
	v_mul_f32_e32 v10, v10, v11
	v_cvt_pk_bf16_f32 v10, v10, s0
	v_mul_f32_e32 v6, v6, v11
	v_cvt_pk_bf16_f32 v6, v6, s0
	ds_write_b16 v89, v10 offset:17408
	ds_write_b16 v83, v6 offset:34820
	ds_read_u16 v10, v90 offset:59392
	ds_read_u16 v11, v91
	v_add_f32_e32 v6, v26, v9
	v_exp_f32_e32 v12, v6
	s_waitcnt lgkmcnt(1)
	v_lshlrev_b32_e32 v10, 16, v10
	v_mul_f32_e32 v10, 0x3db504f3, v10
	v_mul_f32_e32 v10, v12, v10
	v_cvt_pk_bf16_f32 v10, v10, s0
	ds_write_b16 v92, v10
	v_exp_f32_e64 v10, -v6
	v_sub_f32_e32 v6, v7, v6
	v_exp_f32_e32 v6, v6
	s_waitcnt lgkmcnt(1)
	v_lshlrev_b32_e32 v11, 16, v11
	v_mul_f32_e32 v10, v10, v11
	v_cvt_pk_bf16_f32 v10, v10, s0
	v_mul_f32_e32 v6, v6, v11
	v_cvt_pk_bf16_f32 v6, v6, s0
	ds_write_b16 v92, v10 offset:17408
	ds_write_b16 v83, v6 offset:34822
	ds_read_u16 v10, v93 offset:59392
	ds_read_u16 v11, v94
	v_add_f32_e32 v6, v27, v9
	v_exp_f32_e32 v12, v6
	s_waitcnt lgkmcnt(1)
	v_lshlrev_b32_e32 v10, 16, v10
	v_mul_f32_e32 v10, 0x3db504f3, v10
	v_mul_f32_e32 v10, v12, v10
	v_cvt_pk_bf16_f32 v10, v10, s0
	ds_write_b16 v95, v10
	v_exp_f32_e64 v10, -v6
	v_sub_f32_e32 v6, v7, v6
	v_exp_f32_e32 v6, v6
	s_waitcnt lgkmcnt(1)
	v_lshlrev_b32_e32 v11, 16, v11
	v_mul_f32_e32 v10, v10, v11
	v_cvt_pk_bf16_f32 v10, v10, s0
	v_mul_f32_e32 v6, v6, v11
	v_cvt_pk_bf16_f32 v6, v6, s0
	ds_write_b16 v95, v10 offset:17408
	ds_write_b16 v83, v6 offset:34824
	ds_read_u16 v10, v96 offset:59392
	ds_read_u16 v11, v97
	v_add_f32_e32 v6, v28, v9
	v_exp_f32_e32 v12, v6
	s_waitcnt lgkmcnt(1)
	v_lshlrev_b32_e32 v10, 16, v10
	v_mul_f32_e32 v10, 0x3db504f3, v10
	v_mul_f32_e32 v10, v12, v10
	v_cvt_pk_bf16_f32 v10, v10, s0
	ds_write_b16 v98, v10
	v_exp_f32_e64 v10, -v6
	v_sub_f32_e32 v6, v7, v6
	v_exp_f32_e32 v6, v6
	s_waitcnt lgkmcnt(1)
	v_lshlrev_b32_e32 v11, 16, v11
	v_mul_f32_e32 v10, v10, v11
	v_cvt_pk_bf16_f32 v10, v10, s0
	v_mul_f32_e32 v6, v6, v11
	v_cvt_pk_bf16_f32 v6, v6, s0
	ds_write_b16 v98, v10 offset:17408
	ds_write_b16 v83, v6 offset:34826
	ds_read_u16 v10, v99 offset:59392
	ds_read_u16 v11, v100
	v_add_f32_e32 v6, v29, v9
	v_exp_f32_e32 v12, v6
	s_waitcnt lgkmcnt(1)
	v_lshlrev_b32_e32 v10, 16, v10
	v_mul_f32_e32 v10, 0x3db504f3, v10
	v_mul_f32_e32 v10, v12, v10
	v_cvt_pk_bf16_f32 v10, v10, s0
	ds_write_b16 v101, v10
	v_exp_f32_e64 v10, -v6
	v_sub_f32_e32 v6, v7, v6
	v_exp_f32_e32 v6, v6
	s_waitcnt lgkmcnt(1)
	v_lshlrev_b32_e32 v11, 16, v11
	v_mul_f32_e32 v10, v10, v11
	v_cvt_pk_bf16_f32 v10, v10, s0
	v_mul_f32_e32 v6, v6, v11
	v_cvt_pk_bf16_f32 v6, v6, s0
	ds_write_b16 v101, v10 offset:17408
	ds_write_b16 v83, v6 offset:34828
	ds_read_u16 v10, v102 offset:59392
	ds_read_u16 v11, v103
	v_add_f32_e32 v6, v30, v9
	v_exp_f32_e32 v12, v6
	s_waitcnt lgkmcnt(1)
	v_lshlrev_b32_e32 v10, 16, v10
	v_mul_f32_e32 v10, 0x3db504f3, v10
	v_mul_f32_e32 v10, v12, v10
	v_cvt_pk_bf16_f32 v10, v10, s0
	ds_write_b16 v104, v10
	v_exp_f32_e64 v10, -v6
	v_sub_f32_e32 v6, v7, v6
	v_exp_f32_e32 v6, v6
	s_waitcnt lgkmcnt(1)
	v_lshlrev_b32_e32 v11, 16, v11
	v_mul_f32_e32 v10, v10, v11
	v_cvt_pk_bf16_f32 v10, v10, s0
	v_mul_f32_e32 v6, v6, v11
	v_cvt_pk_bf16_f32 v6, v6, s0
	ds_write_b16 v104, v10 offset:17408
	ds_write_b16 v83, v6 offset:34830
	ds_read_u16 v10, v105 offset:59392
	ds_read_u16 v11, v106
	v_add_f32_e32 v6, v31, v9
	v_exp_f32_e32 v12, v6
	s_waitcnt lgkmcnt(1)
	v_lshlrev_b32_e32 v10, 16, v10
	v_mul_f32_e32 v10, 0x3db504f3, v10
	v_mul_f32_e32 v10, v12, v10
	v_cvt_pk_bf16_f32 v10, v10, s0
	ds_write_b16 v107, v10
	v_exp_f32_e64 v10, -v6
	v_sub_f32_e32 v6, v7, v6
	v_exp_f32_e32 v6, v6
	s_waitcnt lgkmcnt(1)
	v_lshlrev_b32_e32 v11, 16, v11
	v_mul_f32_e32 v10, v10, v11
	v_cvt_pk_bf16_f32 v10, v10, s0
	v_mul_f32_e32 v6, v6, v11
	v_cvt_pk_bf16_f32 v6, v6, s0
	ds_write_b16 v107, v10 offset:17408
	ds_write_b16 v83, v6 offset:34832
	ds_read_u16 v10, v108 offset:59392
	ds_read_u16 v11, v109
	v_add_f32_e32 v6, v32, v9
	v_exp_f32_e32 v12, v6
	s_waitcnt lgkmcnt(1)
	v_lshlrev_b32_e32 v10, 16, v10
	v_mul_f32_e32 v10, 0x3db504f3, v10
	v_mul_f32_e32 v10, v12, v10
	v_cvt_pk_bf16_f32 v10, v10, s0
	ds_write_b16 v110, v10
	v_exp_f32_e64 v10, -v6
	v_sub_f32_e32 v6, v7, v6
	v_exp_f32_e32 v6, v6
	s_waitcnt lgkmcnt(1)
	v_lshlrev_b32_e32 v11, 16, v11
	v_mul_f32_e32 v10, v10, v11
	v_cvt_pk_bf16_f32 v10, v10, s0
	v_mul_f32_e32 v6, v6, v11
	v_cvt_pk_bf16_f32 v6, v6, s0
	ds_write_b16 v110, v10 offset:17408
	ds_write_b16 v83, v6 offset:34834
	ds_read_u16 v10, v111 offset:59392
	ds_read_u16 v11, v112
	v_add_f32_e32 v6, v33, v9
	v_exp_f32_e32 v12, v6
	s_waitcnt lgkmcnt(1)
	v_lshlrev_b32_e32 v10, 16, v10
	v_mul_f32_e32 v10, 0x3db504f3, v10
	v_mul_f32_e32 v10, v12, v10
	v_cvt_pk_bf16_f32 v10, v10, s0
	ds_write_b16 v113, v10
	v_exp_f32_e64 v10, -v6
	v_sub_f32_e32 v6, v7, v6
	v_exp_f32_e32 v6, v6
	s_waitcnt lgkmcnt(1)
	v_lshlrev_b32_e32 v11, 16, v11
	v_mul_f32_e32 v10, v10, v11
	v_cvt_pk_bf16_f32 v10, v10, s0
	v_mul_f32_e32 v6, v6, v11
	v_cvt_pk_bf16_f32 v6, v6, s0
	ds_write_b16 v113, v10 offset:17408
	ds_write_b16 v83, v6 offset:34836
	ds_read_u16 v10, v114 offset:59392
	ds_read_u16 v11, v115
	v_add_f32_e32 v6, v63, v9
	v_exp_f32_e32 v12, v6
	s_waitcnt lgkmcnt(1)
	v_lshlrev_b32_e32 v10, 16, v10
	v_mul_f32_e32 v10, 0x3db504f3, v10
	v_mul_f32_e32 v10, v12, v10
	v_cvt_pk_bf16_f32 v10, v10, s0
	ds_write_b16 v116, v10
	v_exp_f32_e64 v10, -v6
	v_sub_f32_e32 v6, v7, v6
	v_exp_f32_e32 v6, v6
	s_waitcnt lgkmcnt(1)
	v_lshlrev_b32_e32 v11, 16, v11
	v_mul_f32_e32 v10, v10, v11
	v_cvt_pk_bf16_f32 v10, v10, s0
	v_mul_f32_e32 v6, v6, v11
	v_cvt_pk_bf16_f32 v6, v6, s0
	ds_write_b16 v116, v10 offset:17408
	ds_write_b16 v83, v6 offset:34838
	ds_read_u16 v10, v117 offset:59392
	ds_read_u16 v11, v118
	v_add_f32_e32 v6, v64, v9
	v_exp_f32_e32 v12, v6
	s_waitcnt lgkmcnt(1)
	v_lshlrev_b32_e32 v10, 16, v10
	v_mul_f32_e32 v10, 0x3db504f3, v10
	v_mul_f32_e32 v10, v12, v10
	v_cvt_pk_bf16_f32 v10, v10, s0
	ds_write_b16 v119, v10
	v_exp_f32_e64 v10, -v6
	v_sub_f32_e32 v6, v7, v6
	v_exp_f32_e32 v6, v6
	s_waitcnt lgkmcnt(1)
	v_lshlrev_b32_e32 v11, 16, v11
	v_mul_f32_e32 v10, v10, v11
	v_cvt_pk_bf16_f32 v10, v10, s0
	v_mul_f32_e32 v6, v6, v11
	v_cvt_pk_bf16_f32 v6, v6, s0
	ds_write_b16 v119, v10 offset:17408
	ds_write_b16 v83, v6 offset:34840
	ds_read_u16 v10, v120 offset:59392
	ds_read_u16 v11, v121
	v_add_f32_e32 v6, v65, v9
	v_exp_f32_e32 v12, v6
	s_waitcnt lgkmcnt(1)
	v_lshlrev_b32_e32 v10, 16, v10
	v_mul_f32_e32 v10, 0x3db504f3, v10
	v_mul_f32_e32 v10, v12, v10
	v_cvt_pk_bf16_f32 v10, v10, s0
	ds_write_b16 v122, v10
	v_exp_f32_e64 v10, -v6
	v_sub_f32_e32 v6, v7, v6
	v_exp_f32_e32 v6, v6
	s_waitcnt lgkmcnt(1)
	v_lshlrev_b32_e32 v11, 16, v11
	v_mul_f32_e32 v10, v10, v11
	v_cvt_pk_bf16_f32 v10, v10, s0
	v_mul_f32_e32 v6, v6, v11
	v_cvt_pk_bf16_f32 v6, v6, s0
	ds_write_b16 v122, v10 offset:17408
	ds_write_b16 v83, v6 offset:34842
	ds_read_u16 v10, v123 offset:59392
	ds_read_u16 v11, v124
	v_add_f32_e32 v6, v66, v9
	v_exp_f32_e32 v12, v6
	s_waitcnt lgkmcnt(1)
	v_lshlrev_b32_e32 v10, 16, v10
	v_mul_f32_e32 v10, 0x3db504f3, v10
	v_mul_f32_e32 v10, v12, v10
	v_cvt_pk_bf16_f32 v10, v10, s0
	ds_write_b16 v125, v10
	v_exp_f32_e64 v10, -v6
	v_sub_f32_e32 v6, v7, v6
	v_exp_f32_e32 v6, v6
	s_waitcnt lgkmcnt(1)
	v_lshlrev_b32_e32 v11, 16, v11
	v_mul_f32_e32 v10, v10, v11
	v_cvt_pk_bf16_f32 v10, v10, s0
	v_mul_f32_e32 v6, v6, v11
	v_cvt_pk_bf16_f32 v6, v6, s0
	ds_write_b16 v125, v10 offset:17408
	ds_write_b16 v83, v6 offset:34844
	v_add_f32_e32 v6, v9, v8
	ds_read_u16 v8, v126 offset:59392
	ds_read_u16 v9, v127
	v_exp_f32_e32 v10, v6
	s_waitcnt lgkmcnt(1)
	v_lshlrev_b32_e32 v8, 16, v8
	v_mul_f32_e32 v8, 0x3db504f3, v8
	v_mul_f32_e32 v8, v10, v8
	v_cvt_pk_bf16_f32 v8, v8, s0
	ds_write_b16 v128, v8
	v_exp_f32_e64 v8, -v6
	v_sub_f32_e32 v6, v7, v6
	v_exp_f32_e32 v6, v6
	s_waitcnt lgkmcnt(1)
	v_lshlrev_b32_e32 v9, 16, v9
	v_mul_f32_e32 v8, v8, v9
	v_cvt_pk_bf16_f32 v8, v8, s0
	v_mul_f32_e32 v6, v6, v9
	v_cvt_pk_bf16_f32 v6, v6, s0
	ds_write_b16 v128, v8 offset:17408
	ds_write_b16 v83, v6 offset:34846
	s_mov_b64 s[14:15], exec
	v_readlane_b32 vcc_lo, v254, 60
	v_readlane_b32 vcc_hi, v254, 61
	s_and_b64 vcc, s[14:15], vcc
	s_xor_b64 s[14:15], vcc, s[14:15]
	s_mov_b64 exec, vcc
	s_ashr_i32 s11, s10, 31
	s_or_saveexec_b64 s[14:15], s[14:15]
	v_mov_b64_e32 v[64:65], s[10:11]
	s_xor_b64 exec, exec, s[14:15]
	s_cbranch_execz .LBB0_287
	v_exp_f32_e32 v8, v7
	s_ashr_i32 s11, s10, 31
	s_lshl_b64 vcc, s[10:11], 9
	v_lshl_add_u64 v[6:7], v[36:37], 0, vcc
	v_mov_b64_e32 v[64:65], s[10:11]
	global_store_dword v[6:7], v8, off
	s_branch .LBB0_287
